# Prologue: converted weights that are first needed much later (W_in layer 1, Wa/Wb, W_out) are stored with the nt hint; layer-0 W_in keeps the default policy
# baseline (speedup 1.0000x reference)
; __device__ __forceinline__ unsigned cvt_pk_bf16(float lo, float hi) { f32x2_t v = {lo, hi}; bf16x2_t b = __builtin_convertvector(v, bf16x2_t); return __builtin_bit_cast(unsigned, b); }
;     const int c = lane & 7, nn = lane >> 3;
;     const float* src0 = W + (size_t)(kb * 64 + 8 * c) * ldw;
; #pragma unroll 2
;     for (int sb = sb0; sb < sb1; ++sb) {
;         const int n = nb * 256 + sb * 32 + 4 * nn;
;         if (n < N) {
;             int r = n;
;             if (rowmode == 1) r = n < 2608 ? n : n + 208;
;             else if (rowmode == 2) r = ((n >> 7) << 8) + (n & 127);
;             else if (rowmode == 3) r = ((n >> 7) << 8) + 128 + (n & 127);
;             const float* src = src0 + n;
;             f32x4 v[8];
; #pragma unroll
;             for (int i = 0; i < 8; ++i) v[i] = *(const f32x4*)(src + (size_t)i * ldw);
;             bf16* d0 = WT + (size_t)r * K + kb * 64 + 8 * c;
; #pragma unroll
;             for (int j = 0; j < 4; ++j) { u32x4 o; o.x = cvt_pk_bf16(v[0][j], v[1][j]); o.y = cvt_pk_bf16(v[2][j], v[3][j]); o.z = cvt_pk_bf16(v[4][j], v[5][j]); o.w = cvt_pk_bf16(v[6][j], v[7][j]);
;                 *(u32x4*)(d0 + (size_t)j * K) = o; }
;         }
;     }
; }
; __global__ void __launch_bounds__(NWAVES * 64, 2) trunk_fwd(Args args) {
;     ...
;                 if (r < C_WO) { const int l = r / (32 * 8), q = r % (32 * 8); conv_tile(args.in[I_WO] + (size_t)l * 2048 * 2048, 2048, 2048, 2048, WO_T + (size_t)l * 2048 * 2048, 0, q / 8, q % 8, lane, wave, wave + 1); continue; } r -= C_WO;
.LBB0_46:
	s_andn2_b64 vcc, exec, s[20:21]
	s_cbranch_vccnz .LBB0_49
	s_and_b32 s2, s31, 0x700
	s_add_i32 s20, s30, s2
	s_cmpk_gt_u32 s20, 0x7ff
	s_cbranch_scc1 .LBB0_49
	s_add_i32 s2, s67, 0xfffff540
	s_lshr_b32 s18, s2, 8
	s_lshl_b64 s[68:69], s[18:19], 23
	s_add_u32 s2, s26, s68
	s_addc_u32 s21, s27, s69
	s_add_i32 s68, s66, 0xffffaa00
	s_and_b32 s70, s68, 0x7c0
	s_lshl_b32 s68, s70, 1
	s_add_u32 s68, s2, s68
	s_addc_u32 s69, s21, 0
	v_lshlrev_b32_e32 v4, 1, v2
	v_lshl_add_u64 v[50:51], s[68:69], 0, v[4:5]
	s_lshl_b64 s[68:69], s[18:19], 24
	s_waitcnt lgkmcnt(0)
	s_add_u32 s68, s6, s68
	v_or_b32_e32 v4, s70, v2
	s_addc_u32 s69, s7, s69
	v_lshlrev_b32_e32 v4, 13, v4
	v_lshl_add_u64 v[18:19], s[68:69], 0, v[4:5]
	v_or_b32_e32 v4, s20, v3
	v_lshl_add_u64 v[42:43], v[4:5], 2, v[18:19]
	v_add_co_u32_e32 v22, vcc, s37, v42
	v_lshlrev_b64 v[52:53], 12, v[4:5]
	s_nop 0
	v_addc_co_u32_e32 v23, vcc, 0, v43, vcc
	v_add_co_u32_e32 v26, vcc, s38, v42
	global_load_dwordx4 v[18:21], v[42:43], off nt
	s_nop 0
	global_load_dwordx4 v[22:25], v[22:23], off nt
	v_addc_co_u32_e32 v27, vcc, 0, v43, vcc
	v_add_co_u32_e32 v30, vcc, s39, v42
	v_lshl_add_u64 v[62:63], v[50:51], 0, v[52:53]
	s_nop 0
	v_addc_co_u32_e32 v31, vcc, 0, v43, vcc
	v_add_co_u32_e32 v34, vcc, s40, v42
	global_load_dwordx4 v[26:29], v[26:27], off nt
	s_nop 0
	global_load_dwordx4 v[30:33], v[30:31], off nt
	v_addc_co_u32_e32 v35, vcc, 0, v43, vcc
	v_add_co_u32_e32 v38, vcc, s41, v42
	s_waitcnt vmcnt(2)
	v_cvt_pk_bf16_f32 v50, v18, v22
	v_addc_co_u32_e32 v39, vcc, 0, v43, vcc
	v_add_co_u32_e32 v44, vcc, s42, v42
	global_load_dwordx4 v[34:37], v[34:35], off nt
	s_nop 0
	global_load_dwordx4 v[38:41], v[38:39], off nt
	v_addc_co_u32_e32 v45, vcc, 0, v43, vcc
	v_add_co_u32_e32 v46, vcc, s43, v42
	s_waitcnt vmcnt(2)
	v_cvt_pk_bf16_f32 v51, v26, v30
	v_addc_co_u32_e32 v47, vcc, 0, v43, vcc
	global_load_dwordx4 v[42:45], v[44:45], off nt
	s_nop 0
	global_load_dwordx4 v[46:49], v[46:47], off nt
	v_add_co_u32_e32 v64, vcc, s37, v62
	v_cvt_pk_bf16_f32 v54, v19, v23
	s_nop 0
	v_addc_co_u32_e32 v65, vcc, 0, v63, vcc
	v_add_co_u32_e32 v66, vcc, 0x3000, v62
	v_cvt_pk_bf16_f32 v55, v27, v31
	s_nop 0
	v_addc_co_u32_e32 v67, vcc, 0, v63, vcc
	v_cvt_pk_bf16_f32 v58, v20, v24
	v_cvt_pk_bf16_f32 v59, v28, v32
	v_cvt_pk_bf16_f32 v18, v21, v25
	v_cvt_pk_bf16_f32 v19, v29, v33
	s_waitcnt vmcnt(2)
	v_cvt_pk_bf16_f32 v52, v34, v38
	v_cvt_pk_bf16_f32 v56, v35, v39
	v_cvt_pk_bf16_f32 v60, v36, v40
	v_cvt_pk_bf16_f32 v20, v37, v41
	s_waitcnt vmcnt(0)
	v_cvt_pk_bf16_f32 v53, v42, v46
	v_cvt_pk_bf16_f32 v57, v43, v47
	v_cvt_pk_bf16_f32 v61, v44, v48
	v_cvt_pk_bf16_f32 v21, v45, v49
	global_store_dwordx4 v[62:63], v[50:53], off nt
	global_store_dwordx4 v[64:65], v[54:57], off offset:-4096 nt
	global_store_dwordx4 v[64:65], v[58:61], off nt
	global_store_dwordx4 v[66:67], v[18:21], off nt

; __device__ __forceinline__ unsigned cvt_pk_bf16(float lo, float hi) { f32x2_t v = {lo, hi}; bf16x2_t b = __builtin_convertvector(v, bf16x2_t); return __builtin_bit_cast(unsigned, b); }
;     const int c = lane & 7, nn = lane >> 3;
;     const float* src0 = W + (size_t)(kb * 64 + 8 * c) * ldw;
; #pragma unroll 2
;     for (int sb = sb0; sb < sb1; ++sb) {
;         const int n = nb * 256 + sb * 32 + 4 * nn;
;         if (n < N) {
;             int r = n;
;             if (rowmode == 1) r = n < 2608 ? n : n + 208;
;             else if (rowmode == 2) r = ((n >> 7) << 8) + (n & 127);
;             else if (rowmode == 3) r = ((n >> 7) << 8) + 128 + (n & 127);
;             const float* src = src0 + n;
;             f32x4 v[8];
; #pragma unroll
;             for (int i = 0; i < 8; ++i) v[i] = *(const f32x4*)(src + (size_t)i * ldw);
;             bf16* d0 = WT + (size_t)r * K + kb * 64 + 8 * c;
; #pragma unroll
;             for (int j = 0; j < 4; ++j) { u32x4 o; o.x = cvt_pk_bf16(v[0][j], v[1][j]); o.y = cvt_pk_bf16(v[2][j], v[3][j]); o.z = cvt_pk_bf16(v[4][j], v[5][j]); o.w = cvt_pk_bf16(v[6][j], v[7][j]);
;                 *(u32x4*)(d0 + (size_t)j * K) = o; }
;         }
;     }
; }
; __global__ void __launch_bounds__(NWAVES * 64, 2) trunk_fwd(Args args) {
;     ...
;                 if (r < C_WAB) { const int ab = r / (2 * 16 * 8), l = (r / (16 * 8)) & 1, q = r % (16 * 8); conv_tile(args.in[ab ? I_WB : I_WA] + (size_t)l * 1024 * 2048, 2048, 1024, 2048, (ab ? WB_T : WA_T) + (size_t)l * 2048 * 1024, 0, q / 8, q % 8, lane, wave, wave + 1); continue; } r -= C_WAB;
.LBB0_50:
	s_andn2_b64 vcc, exec, s[20:21]
	s_cbranch_vccnz .LBB0_53
	s_and_b32 s2, s31, 0x700
	s_add_i32 s18, s30, s2
	s_cmpk_gt_u32 s18, 0x7ff
	s_cbranch_scc1 .LBB0_53
	s_load_dwordx2 s[70:71], s[0:1], 0xd8
	s_add_i32 s2, s67, 0xfffff740
	s_cmpk_lt_u32 s2, 0x100
	s_cselect_b32 s20, s56, 0x5321000
	s_cselect_b32 s68, s57, 0x70
	s_waitcnt lgkmcnt(0)
	s_add_u32 s20, s70, s20
	s_addc_u32 s21, s71, 0
	s_bfe_u32 s2, s2, 0x10007
	s_lshl_b32 s69, s2, 22
	s_add_u32 s20, s20, s69
	s_addc_u32 s21, s21, 0
	s_add_i32 s69, s66, 0xffffba00
	s_and_b32 s70, s69, 0x3c0
	s_lshl_b32 s69, s70, 1
	s_add_u32 s20, s20, s69
	s_addc_u32 s21, s21, 0
	s_add_u32 s68, s0, s68
	s_addc_u32 s69, s1, 0
	s_load_dwordx2 s[68:69], s[68:69], 0x0
	v_lshlrev_b32_e32 v4, 1, v2
	s_lshl_b32 s2, s2, 23
	v_lshl_add_u64 v[50:51], s[20:21], 0, v[4:5]
	v_or_b32_e32 v4, s70, v2
	s_waitcnt lgkmcnt(0)
	s_add_u32 s20, s68, s2
	s_addc_u32 s21, s69, 0
	v_lshlrev_b32_e32 v4, 13, v4
	v_lshl_add_u64 v[18:19], s[20:21], 0, v[4:5]
	v_or_b32_e32 v4, s18, v3
	v_lshl_add_u64 v[42:43], v[4:5], 2, v[18:19]
	v_add_co_u32_e32 v22, vcc, s37, v42
	v_lshlrev_b64 v[52:53], 11, v[4:5]
	s_nop 0
	v_addc_co_u32_e32 v23, vcc, 0, v43, vcc
	v_add_co_u32_e32 v26, vcc, s38, v42
	global_load_dwordx4 v[18:21], v[42:43], off nt
	s_nop 0
	global_load_dwordx4 v[22:25], v[22:23], off nt
	v_addc_co_u32_e32 v27, vcc, 0, v43, vcc
	v_add_co_u32_e32 v30, vcc, s39, v42
	v_lshl_add_u64 v[62:63], v[50:51], 0, v[52:53]
	s_nop 0
	v_addc_co_u32_e32 v31, vcc, 0, v43, vcc
	v_add_co_u32_e32 v34, vcc, s40, v42
	global_load_dwordx4 v[26:29], v[26:27], off nt
	s_nop 0
	global_load_dwordx4 v[30:33], v[30:31], off nt
	v_addc_co_u32_e32 v35, vcc, 0, v43, vcc
	v_add_co_u32_e32 v38, vcc, s41, v42
	s_waitcnt vmcnt(2)
	v_cvt_pk_bf16_f32 v50, v18, v22
	v_addc_co_u32_e32 v39, vcc, 0, v43, vcc
	v_add_co_u32_e32 v44, vcc, s42, v42
	global_load_dwordx4 v[34:37], v[34:35], off nt
	s_nop 0
	global_load_dwordx4 v[38:41], v[38:39], off nt
	v_addc_co_u32_e32 v45, vcc, 0, v43, vcc
	v_add_co_u32_e32 v46, vcc, s43, v42
	s_waitcnt vmcnt(2)
	v_cvt_pk_bf16_f32 v51, v26, v30
	v_addc_co_u32_e32 v47, vcc, 0, v43, vcc
	global_load_dwordx4 v[42:45], v[44:45], off nt
	s_nop 0
	global_load_dwordx4 v[46:49], v[46:47], off nt
	v_add_co_u32_e32 v64, vcc, s55, v62
	v_cvt_pk_bf16_f32 v54, v19, v23
	s_nop 0
	v_addc_co_u32_e32 v65, vcc, 0, v63, vcc
	v_cvt_pk_bf16_f32 v55, v27, v31
	v_cvt_pk_bf16_f32 v58, v20, v24
	v_cvt_pk_bf16_f32 v59, v28, v32
	v_cvt_pk_bf16_f32 v18, v21, v25
	v_cvt_pk_bf16_f32 v19, v29, v33
	s_waitcnt vmcnt(2)
	v_cvt_pk_bf16_f32 v52, v34, v38
	v_cvt_pk_bf16_f32 v56, v35, v39
	v_cvt_pk_bf16_f32 v60, v36, v40
	v_cvt_pk_bf16_f32 v20, v37, v41
	s_waitcnt vmcnt(0)
	v_cvt_pk_bf16_f32 v53, v42, v46
	v_cvt_pk_bf16_f32 v57, v43, v47
	v_cvt_pk_bf16_f32 v61, v44, v48
	v_cvt_pk_bf16_f32 v21, v45, v49
	global_store_dwordx4 v[62:63], v[50:53], off nt
	global_store_dwordx4 v[62:63], v[54:57], off offset:2048 nt
	global_store_dwordx4 v[64:65], v[58:61], off nt
	global_store_dwordx4 v[64:65], v[18:21], off offset:2048 nt

; __device__ __forceinline__ unsigned cvt_pk_bf16(float lo, float hi) { f32x2_t v = {lo, hi}; bf16x2_t b = __builtin_convertvector(v, bf16x2_t); return __builtin_bit_cast(unsigned, b); }
;     const int c = lane & 7, nn = lane >> 3;
;     const float* src0 = W + (size_t)(kb * 64 + 8 * c) * ldw;
; #pragma unroll 2
;     for (int sb = sb0; sb < sb1; ++sb) {
;         const int n = nb * 256 + sb * 32 + 4 * nn;
;         if (n < N) {
;             int r = n;
;             if (rowmode == 1) r = n < 2608 ? n : n + 208;
;             else if (rowmode == 2) r = ((n >> 7) << 8) + (n & 127);
;             else if (rowmode == 3) r = ((n >> 7) << 8) + 128 + (n & 127);
;             const float* src = src0 + n;
;             f32x4 v[8];
; #pragma unroll
;             for (int i = 0; i < 8; ++i) v[i] = *(const f32x4*)(src + (size_t)i * ldw);
;             bf16* d0 = WT + (size_t)r * K + kb * 64 + 8 * c;
; #pragma unroll
;             for (int j = 0; j < 4; ++j) { u32x4 o; o.x = cvt_pk_bf16(v[0][j], v[1][j]); o.y = cvt_pk_bf16(v[2][j], v[3][j]); o.z = cvt_pk_bf16(v[4][j], v[5][j]); o.w = cvt_pk_bf16(v[6][j], v[7][j]);
;                 *(u32x4*)(d0 + (size_t)j * K) = o; }
;         }
;     }
; }
; __global__ void __launch_bounds__(NWAVES * 64, 2) trunk_fwd(Args args) {
;     ...
;                 if (r < C_WIN) { const int l = r / (32 * 35), q = r % (32 * 35); conv_tile(args.in[I_WIN] + (size_t)l * D * IN_W, IN_W, D, IN_W, WIN_T + (size_t)l * ZLD * D, 1, q / 35, q % 35, lane, wave, wave + 1); continue; } r -= C_WIN;
.LBB0_54:
	s_andn2_b64 vcc, exec, s[20:21]
	s_cbranch_vccnz .LBB0_24
	s_mul_hi_i32 s2, s67, 0xea0ea0eb
	s_add_i32 s2, s2, s67
	s_lshr_b32 s18, s2, 31
	s_ashr_i32 s2, s2, 10
	s_add_i32 s18, s2, s18
	s_mul_i32 s2, s18, 0xfffffba0
	s_add_i32 s2, s67, s2
	s_mul_i32 s20, s2, 0xea1
	s_lshr_b32 s21, s20, 31
	s_ashr_i32 s68, s20, 17
	s_add_i32 s68, s68, s21
	s_mul_i32 s20, s68, 35
	s_sub_i32 s2, s2, s20
	s_sext_i32_i16 s2, s2
	s_lshl_b32 s69, s2, 8
	v_add_u32_e32 v17, s69, v10
	v_cmp_gt_i32_e32 vcc, s58, v17
	s_and_saveexec_b64 s[20:21], vcc
	s_cbranch_execz .LBB0_23
	v_or_b32_e32 v4, s69, v3
	s_mul_i32 s69, s18, 0x2300000
	s_mul_hi_i32 s2, s18, 0x2300000
	s_add_u32 s72, s28, s69
	s_sext_i32_i16 s68, s68
	s_addc_u32 s2, s29, s2
	s_lshl_b32 s68, s68, 6
	s_ashr_i32 s69, s68, 31
	s_lshl_b64 s[70:71], s[68:69], 1
	s_add_u32 s70, s72, s70
	v_add_u32_e32 v50, s30, v4
	s_addc_u32 s71, s2, s71
	s_mul_hi_i32 s2, s18, 0x4460000
	s_mul_i32 s18, s18, 0x4460000
	v_or_b32_e32 v4, s68, v2
	s_waitcnt lgkmcnt(0)
	s_add_u32 s72, s12, s18
	v_mul_i32_i24_e32 v18, 0x2230, v4
	s_addc_u32 s73, s13, s2
	v_ashrrev_i32_e32 v19, 31, v18
	v_lshl_add_u64 v[18:19], v[18:19], 2, s[72:73]
	v_ashrrev_i32_e32 v51, 31, v50
	v_lshl_add_u64 v[42:43], v[50:51], 2, v[18:19]
	v_add_co_u32_e32 v22, vcc, s40, v42
	v_add_u32_e32 v51, 0xd0, v50
	s_nop 0
	v_addc_co_u32_e32 v23, vcc, 0, v43, vcc
	v_add_co_u32_e32 v26, vcc, s60, v42
	global_load_dwordx4 v[18:21], v[42:43], off nt
	s_nop 0
	global_load_dwordx4 v[22:25], v[22:23], off offset:2240 nt
	v_addc_co_u32_e32 v27, vcc, 0, v43, vcc
	v_add_co_u32_e32 v30, vcc, s61, v42
	v_lshlrev_b32_e32 v4, 1, v2
	s_nop 0
	v_addc_co_u32_e32 v31, vcc, 0, v43, vcc
	v_add_co_u32_e32 v34, vcc, s62, v42
	global_load_dwordx4 v[26:29], v[26:27], off offset:384 nt
	s_nop 0
	global_load_dwordx4 v[30:33], v[30:31], off offset:2624 nt
	v_addc_co_u32_e32 v35, vcc, 0, v43, vcc
	v_add_co_u32_e32 v38, vcc, s63, v42
	v_lshl_add_u64 v[52:53], s[70:71], 0, v[4:5]
	s_nop 0
	v_addc_co_u32_e32 v39, vcc, 0, v43, vcc
	v_add_co_u32_e32 v44, vcc, s64, v42
	global_load_dwordx4 v[34:37], v[34:35], off offset:768 nt
	s_nop 0
	global_load_dwordx4 v[38:41], v[38:39], off offset:3008 nt
	v_addc_co_u32_e32 v45, vcc, 0, v43, vcc
	v_add_co_u32_e32 v46, vcc, s65, v42
	s_waitcnt vmcnt(4)
	v_cvt_pk_bf16_f32 v54, v19, v23
	v_addc_co_u32_e32 v47, vcc, 0, v43, vcc
	global_load_dwordx4 v[42:45], v[44:45], off offset:1152 nt
	s_nop 0
	global_load_dwordx4 v[46:49], v[46:47], off offset:3392 nt
	v_cmp_gt_i32_e32 vcc, s59, v17
	v_cvt_pk_bf16_f32 v58, v20, v24
	s_waitcnt vmcnt(4)
	v_cvt_pk_bf16_f32 v19, v29, v33
	v_cndmask_b32_e32 v50, v51, v50, vcc
	v_ashrrev_i32_e32 v51, 31, v50
	v_lshlrev_b64 v[50:51], 12, v[50:51]
	v_lshl_add_u64 v[62:63], v[52:53], 0, v[50:51]
	v_add_co_u32_e32 v64, vcc, s37, v62
	v_cvt_pk_bf16_f32 v50, v18, v22
	s_nop 0
	v_addc_co_u32_e32 v65, vcc, 0, v63, vcc
	v_add_co_u32_e32 v66, vcc, 0x3000, v62
	v_cvt_pk_bf16_f32 v51, v26, v30
	s_waitcnt vmcnt(2)
	v_cvt_pk_bf16_f32 v52, v34, v38
	v_cvt_pk_bf16_f32 v18, v21, v25
	v_cvt_pk_bf16_f32 v20, v37, v41
	v_addc_co_u32_e32 v67, vcc, 0, v63, vcc
	v_cvt_pk_bf16_f32 v55, v27, v31
	v_cvt_pk_bf16_f32 v56, v35, v39
	v_cvt_pk_bf16_f32 v59, v28, v32
	v_cvt_pk_bf16_f32 v60, v36, v40
	s_waitcnt vmcnt(0)
	v_cvt_pk_bf16_f32 v53, v42, v46
	v_cvt_pk_bf16_f32 v21, v45, v49
	v_cvt_pk_bf16_f32 v57, v43, v47
	v_cvt_pk_bf16_f32 v61, v44, v48
	s_cmpk_lt_u32 s67, 0x460
	s_cbranch_scc1 .Lprol_win_l0
	global_store_dwordx4 v[62:63], v[50:53], off nt
	global_store_dwordx4 v[64:65], v[54:57], off offset:-4096 nt
	global_store_dwordx4 v[64:65], v[58:61], off nt
	global_store_dwordx4 v[66:67], v[18:21], off nt
	s_branch .LBB0_23
.Lprol_win_l0:
	global_store_dwordx4 v[62:63], v[50:53], off
	global_store_dwordx4 v[64:65], v[54:57], off offset:-4096
	global_store_dwordx4 v[64:65], v[58:61], off
	global_store_dwordx4 v[66:67], v[18:21], off
	s_branch .LBB0_23
